# ssm_final carry (Horner) loop: loads batched 16/8/4/2/1 with counted vmcnt instead of one round trip per chunk
# speedup vs baseline: 1.0080x; 1.0080x over previous
.LBB0_527:
	s_or_b64 exec, exec, s[0:1]
	v_mul_f32_e32 v4, v76, v4
	v_mul_f32_e32 v7, 0x3fb8aa3b, v4
	v_fma_f32 v8, v4, s81, -v7
	v_rndne_f32_e32 v11, v7
	v_fmac_f32_e32 v8, 0x32a5705f, v4
	v_sub_f32_e32 v7, v7, v11
	v_add_f32_e32 v7, v7, v8
	v_exp_f32_e32 v7, v7
	v_cvt_i32_f32_e32 v8, v11
	v_cmp_ngt_f32_e32 vcc, s86, v4
	s_brev_b32 s0, 1
	v_lshlrev_b32_e32 v80, 4, v0
	v_ldexp_f32 v7, v7, v8
	v_cndmask_b32_e32 v7, 0, v7, vcc
	v_cmp_nlt_f32_e32 vcc, s92, v4
	v_lshlrev_b32_e32 v2, 4, v2
	v_or_b32_e32 v78, v80, v92
	v_cndmask_b32_e32 v4, v221, v7, vcc
	v_mul_f32_e32 v7, v6, v6
	v_fmamk_f32 v8, v7, 0xb94c1982, v253
	v_fmaak_f32 v8, v7, v8, 0xbe2aaa9d
	v_mul_f32_e32 v8, v7, v8
	v_fmac_f32_e32 v6, v6, v8
	v_fmamk_f32 v8, v7, 0x37d75334, v222
	v_fmaak_f32 v8, v7, v8, 0x3d2aabf7
	v_fmaak_f32 v8, v7, v8, 0xbf000004
	v_fma_f32 v7, v7, v8, 1.0
	v_and_b32_e32 v8, 1, v5
	v_cmp_eq_u32_e32 vcc, 0, v8
	v_lshlrev_b32_e32 v5, 30, v5
	v_ashrrev_i32_e32 v79, 31, v78
	v_cndmask_b32_e64 v6, -v6, v7, vcc
	v_bitop3_b32 v5, v5, v6, s0 bitop3:0x6c
	s_movk_i32 s0, 0x1f8
	v_cmp_class_f32_e64 vcc, v1, s0
	v_mov_b32_e32 v7, 0x7fc00000
	v_xor_b32_e32 v1, v3, v1
	v_cndmask_b32_e32 v5, v7, v5, vcc
	v_mul_f32_e32 v72, v4, v5
	v_lshlrev_b32_e32 v5, 5, v84
	v_sub_u32_e32 v82, v90, v5
	v_mul_f32_e32 v5, v10, v10
	v_fmamk_f32 v6, v5, 0xb94c1982, v253
	v_fmaak_f32 v6, v5, v6, 0xbe2aaa9d
	v_mul_f32_e32 v6, v5, v6
	v_fmac_f32_e32 v10, v10, v6
	v_fmamk_f32 v6, v5, 0x37d75334, v222
	v_fmaak_f32 v6, v5, v6, 0x3d2aabf7
	v_fmaak_f32 v6, v5, v6, 0xbf000004
	v_fma_f32 v5, v5, v6, 1.0
	v_and_b32_e32 v6, 1, v9
	v_cmp_eq_u32_e64 s[0:1], 0, v6
	v_lshlrev_b32_e32 v6, 30, v9
	v_and_b32_e32 v6, 0x80000000, v6
	v_cndmask_b32_e64 v5, v5, v10, s[0:1]
	v_xor_b32_e32 v1, v1, v6
	v_xor_b32_e32 v1, v1, v5
	v_cndmask_b32_e32 v1, v7, v1, vcc
	v_ashrrev_i32_e32 v3, 31, v2
	v_mul_f32_e32 v74, v4, v1
	v_lshlrev_b64 v[2:3], 2, v[2:3]
	v_lshlrev_b64 v[0:1], 8, v[78:79]
	v_lshl_add_u64 v[4:5], s[18:19], 0, v[2:3]
	v_lshl_add_u64 v[2:3], s[20:21], 0, v[2:3]
	v_lshl_add_u64 v[0:1], v[64:65], 0, v[0:1]
	flat_load_dwordx4 v[56:59], v[4:5]
	flat_load_dwordx4 v[60:63], v[2:3]
	flat_load_dwordx4 v[48:51], v[4:5] offset:16
	flat_load_dwordx4 v[52:55], v[2:3] offset:16
	flat_load_dwordx4 v[40:43], v[4:5] offset:32
	flat_load_dwordx4 v[44:47], v[2:3] offset:32
	flat_load_dwordx4 v[24:27], v[4:5] offset:48
	flat_load_dwordx4 v[36:39], v[2:3] offset:48
	flat_load_dwordx4 v[32:35], v[0:1]
	flat_load_dwordx4 v[28:31], v[0:1] offset:16
	flat_load_dwordx4 v[20:23], v[0:1] offset:32
	flat_load_dwordx4 v[16:19], v[0:1] offset:48
	flat_load_dwordx4 v[12:15], v[0:1] offset:64
	flat_load_dwordx4 v[8:11], v[0:1] offset:80
	flat_load_dwordx4 v[4:7], v[0:1] offset:96
	s_nop 0
	flat_load_dwordx4 v[0:3], v[0:1] offset:112
	v_lshl_add_u64 v[78:79], v[78:79], 2, s[22:23]
	flat_load_dword v100, v[78:79]
	v_mov_b32_e32 v144, v145
	v_cmp_lt_i32_e32 vcc, 0, v82
	v_mov_b64_e32 v[78:79], v[144:145]
	s_and_saveexec_b64 s[0:1], vcc
	s_cbranch_execz .LBB0_531
	v_add_f32_e32 v73, v72, v72
	v_mul_f32_e32 v71, v74, v74
	v_mul_f32_e32 v73, v73, v74
	v_fma_f32 v71, v72, v72, -v71
	v_mul_f32_e32 v75, v73, v73
	v_fma_f32 v75, v71, v71, -v75
	v_add_f32_e32 v71, v71, v71
	v_mul_f32_e32 v71, v73, v71
	v_mul_f32_e32 v73, v71, v71
	v_fma_f32 v73, v75, v75, -v73
	v_add_f32_e32 v75, v75, v75
	v_mul_f32_e32 v71, v71, v75
	v_mul_f32_e32 v75, v71, v71
	v_fma_f32 v75, v73, v73, -v75
	v_add_f32_e32 v73, v73, v73
	v_mul_f32_e32 v71, v71, v73
	v_mul_f32_e32 v73, v71, v71
	v_fma_f32 v73, v75, v75, -v73
	v_add_f32_e32 v75, v75, v75
	v_mul_f32_e32 v71, v71, v75
	v_mul_f32_e32 v75, v71, v71
	v_ashrrev_i32_e32 v85, 31, v84
	v_fma_f32 v86, v73, v73, -v75
	v_add_f32_e32 v73, v73, v73
	v_lshlrev_b64 v[78:79], 14, v[84:85]
	v_mul_f32_e32 v88, v71, v73
	v_lshl_add_u64 v[84:85], s[24:25], 0, v[78:79]
	v_mov_b32_e32 v78, 0
	v_mov_b32_e32 v87, v86
	v_mov_b32_e32 v89, v88
	s_mov_b64 s[4:5], 0
	v_mov_b32_e32 v144, v91
	v_mov_b32_e32 v71, v82
	v_mov_b32_e32 v79, v78
	v_readfirstlane_b32 s6, v71
	s_nop 3
.Lhorner_16:
	s_cmp_lt_u32 s6, 16
	s_cbranch_scc1 .Lhorner_8
	v_lshl_add_u64 v[180:181], v[144:145], 2, v[84:85]
	v_add_co_u32_e32 v182, vcc, 0x1000, v180
	s_nop 1
	v_addc_co_u32_e32 v183, vcc, 0, v181, vcc
	global_load_dword v147, v[180:181], off
	global_load_dword v146, v[180:181], off offset:256
	global_load_dword v149, v[180:181], off offset:512
	global_load_dword v148, v[180:181], off offset:768
	global_load_dword v151, v[180:181], off offset:1024
	global_load_dword v150, v[180:181], off offset:1280
	global_load_dword v153, v[180:181], off offset:1536
	global_load_dword v152, v[180:181], off offset:1792
	global_load_dword v155, v[180:181], off offset:2048
	global_load_dword v154, v[180:181], off offset:2304
	global_load_dword v157, v[180:181], off offset:2560
	global_load_dword v156, v[180:181], off offset:2816
	global_load_dword v159, v[180:181], off offset:3072
	global_load_dword v158, v[180:181], off offset:3328
	global_load_dword v161, v[180:181], off offset:3584
	global_load_dword v160, v[180:181], off offset:3840
	global_load_dword v163, v[182:183], off
	global_load_dword v162, v[182:183], off offset:256
	global_load_dword v165, v[182:183], off offset:512
	global_load_dword v164, v[182:183], off offset:768
	global_load_dword v167, v[182:183], off offset:1024
	global_load_dword v166, v[182:183], off offset:1280
	global_load_dword v169, v[182:183], off offset:1536
	global_load_dword v168, v[182:183], off offset:1792
	global_load_dword v171, v[182:183], off offset:2048
	global_load_dword v170, v[182:183], off offset:2304
	global_load_dword v173, v[182:183], off offset:2560
	global_load_dword v172, v[182:183], off offset:2816
	global_load_dword v175, v[182:183], off offset:3072
	global_load_dword v174, v[182:183], off offset:3328
	global_load_dword v177, v[182:183], off offset:3584
	global_load_dword v176, v[182:183], off offset:3840
	v_add_u32_e32 v144, 0x800, v144
	v_pk_mul_f32 v[102:103], v[88:89], v[78:79] op_sel:[0,1] op_sel_hi:[1,0]
	v_pk_fma_f32 v[106:107], v[86:87], v[78:79], v[102:103] neg_lo:[0,0,1] neg_hi:[0,0,1]
	v_pk_fma_f32 v[78:79], v[86:87], v[78:79], v[102:103]
	v_mov_b32_e32 v79, v107
	s_waitcnt vmcnt(30)
	v_pk_add_f32 v[78:79], v[78:79], v[146:147]
	v_pk_mul_f32 v[102:103], v[88:89], v[78:79] op_sel:[0,1] op_sel_hi:[1,0]
	v_pk_fma_f32 v[106:107], v[86:87], v[78:79], v[102:103] neg_lo:[0,0,1] neg_hi:[0,0,1]
	v_pk_fma_f32 v[78:79], v[86:87], v[78:79], v[102:103]
	v_mov_b32_e32 v79, v107
	s_waitcnt vmcnt(28)
	v_pk_add_f32 v[78:79], v[78:79], v[148:149]
	v_pk_mul_f32 v[102:103], v[88:89], v[78:79] op_sel:[0,1] op_sel_hi:[1,0]
	v_pk_fma_f32 v[106:107], v[86:87], v[78:79], v[102:103] neg_lo:[0,0,1] neg_hi:[0,0,1]
	v_pk_fma_f32 v[78:79], v[86:87], v[78:79], v[102:103]
	v_mov_b32_e32 v79, v107
	s_waitcnt vmcnt(26)
	v_pk_add_f32 v[78:79], v[78:79], v[150:151]
	v_pk_mul_f32 v[102:103], v[88:89], v[78:79] op_sel:[0,1] op_sel_hi:[1,0]
	v_pk_fma_f32 v[106:107], v[86:87], v[78:79], v[102:103] neg_lo:[0,0,1] neg_hi:[0,0,1]
	v_pk_fma_f32 v[78:79], v[86:87], v[78:79], v[102:103]
	v_mov_b32_e32 v79, v107
	s_waitcnt vmcnt(24)
	v_pk_add_f32 v[78:79], v[78:79], v[152:153]
	v_pk_mul_f32 v[102:103], v[88:89], v[78:79] op_sel:[0,1] op_sel_hi:[1,0]
	v_pk_fma_f32 v[106:107], v[86:87], v[78:79], v[102:103] neg_lo:[0,0,1] neg_hi:[0,0,1]
	v_pk_fma_f32 v[78:79], v[86:87], v[78:79], v[102:103]
	v_mov_b32_e32 v79, v107
	s_waitcnt vmcnt(22)
	v_pk_add_f32 v[78:79], v[78:79], v[154:155]
	v_pk_mul_f32 v[102:103], v[88:89], v[78:79] op_sel:[0,1] op_sel_hi:[1,0]
	v_pk_fma_f32 v[106:107], v[86:87], v[78:79], v[102:103] neg_lo:[0,0,1] neg_hi:[0,0,1]
	v_pk_fma_f32 v[78:79], v[86:87], v[78:79], v[102:103]
	v_mov_b32_e32 v79, v107
	s_waitcnt vmcnt(20)
	v_pk_add_f32 v[78:79], v[78:79], v[156:157]
	v_pk_mul_f32 v[102:103], v[88:89], v[78:79] op_sel:[0,1] op_sel_hi:[1,0]
	v_pk_fma_f32 v[106:107], v[86:87], v[78:79], v[102:103] neg_lo:[0,0,1] neg_hi:[0,0,1]
	v_pk_fma_f32 v[78:79], v[86:87], v[78:79], v[102:103]
	v_mov_b32_e32 v79, v107
	s_waitcnt vmcnt(18)
	v_pk_add_f32 v[78:79], v[78:79], v[158:159]
	v_pk_mul_f32 v[102:103], v[88:89], v[78:79] op_sel:[0,1] op_sel_hi:[1,0]
	v_pk_fma_f32 v[106:107], v[86:87], v[78:79], v[102:103] neg_lo:[0,0,1] neg_hi:[0,0,1]
	v_pk_fma_f32 v[78:79], v[86:87], v[78:79], v[102:103]
	v_mov_b32_e32 v79, v107
	s_waitcnt vmcnt(16)
	v_pk_add_f32 v[78:79], v[78:79], v[160:161]
	v_pk_mul_f32 v[102:103], v[88:89], v[78:79] op_sel:[0,1] op_sel_hi:[1,0]
	v_pk_fma_f32 v[106:107], v[86:87], v[78:79], v[102:103] neg_lo:[0,0,1] neg_hi:[0,0,1]
	v_pk_fma_f32 v[78:79], v[86:87], v[78:79], v[102:103]
	v_mov_b32_e32 v79, v107
	s_waitcnt vmcnt(14)
	v_pk_add_f32 v[78:79], v[78:79], v[162:163]
	v_pk_mul_f32 v[102:103], v[88:89], v[78:79] op_sel:[0,1] op_sel_hi:[1,0]
	v_pk_fma_f32 v[106:107], v[86:87], v[78:79], v[102:103] neg_lo:[0,0,1] neg_hi:[0,0,1]
	v_pk_fma_f32 v[78:79], v[86:87], v[78:79], v[102:103]
	v_mov_b32_e32 v79, v107
	s_waitcnt vmcnt(12)
	v_pk_add_f32 v[78:79], v[78:79], v[164:165]
	v_pk_mul_f32 v[102:103], v[88:89], v[78:79] op_sel:[0,1] op_sel_hi:[1,0]
	v_pk_fma_f32 v[106:107], v[86:87], v[78:79], v[102:103] neg_lo:[0,0,1] neg_hi:[0,0,1]
	v_pk_fma_f32 v[78:79], v[86:87], v[78:79], v[102:103]
	v_mov_b32_e32 v79, v107
	s_waitcnt vmcnt(10)
	v_pk_add_f32 v[78:79], v[78:79], v[166:167]
	v_pk_mul_f32 v[102:103], v[88:89], v[78:79] op_sel:[0,1] op_sel_hi:[1,0]
	v_pk_fma_f32 v[106:107], v[86:87], v[78:79], v[102:103] neg_lo:[0,0,1] neg_hi:[0,0,1]
	v_pk_fma_f32 v[78:79], v[86:87], v[78:79], v[102:103]
	v_mov_b32_e32 v79, v107
	s_waitcnt vmcnt(8)
	v_pk_add_f32 v[78:79], v[78:79], v[168:169]
	v_pk_mul_f32 v[102:103], v[88:89], v[78:79] op_sel:[0,1] op_sel_hi:[1,0]
	v_pk_fma_f32 v[106:107], v[86:87], v[78:79], v[102:103] neg_lo:[0,0,1] neg_hi:[0,0,1]
	v_pk_fma_f32 v[78:79], v[86:87], v[78:79], v[102:103]
	v_mov_b32_e32 v79, v107
	s_waitcnt vmcnt(6)
	v_pk_add_f32 v[78:79], v[78:79], v[170:171]
	v_pk_mul_f32 v[102:103], v[88:89], v[78:79] op_sel:[0,1] op_sel_hi:[1,0]
	v_pk_fma_f32 v[106:107], v[86:87], v[78:79], v[102:103] neg_lo:[0,0,1] neg_hi:[0,0,1]
	v_pk_fma_f32 v[78:79], v[86:87], v[78:79], v[102:103]
	v_mov_b32_e32 v79, v107
	s_waitcnt vmcnt(4)
	v_pk_add_f32 v[78:79], v[78:79], v[172:173]
	v_pk_mul_f32 v[102:103], v[88:89], v[78:79] op_sel:[0,1] op_sel_hi:[1,0]
	v_pk_fma_f32 v[106:107], v[86:87], v[78:79], v[102:103] neg_lo:[0,0,1] neg_hi:[0,0,1]
	v_pk_fma_f32 v[78:79], v[86:87], v[78:79], v[102:103]
	v_mov_b32_e32 v79, v107
	s_waitcnt vmcnt(2)
	v_pk_add_f32 v[78:79], v[78:79], v[174:175]
	v_pk_mul_f32 v[102:103], v[88:89], v[78:79] op_sel:[0,1] op_sel_hi:[1,0]
	v_pk_fma_f32 v[106:107], v[86:87], v[78:79], v[102:103] neg_lo:[0,0,1] neg_hi:[0,0,1]
	v_pk_fma_f32 v[78:79], v[86:87], v[78:79], v[102:103]
	v_mov_b32_e32 v79, v107
	s_waitcnt vmcnt(0)
	v_pk_add_f32 v[78:79], v[78:79], v[176:177]
	s_sub_u32 s6, s6, 16
	s_branch .Lhorner_16
.Lhorner_8:
	s_bitcmp1_b32 s6, 3
	s_cbranch_scc0 .Lhorner_4
	v_lshl_add_u64 v[180:181], v[144:145], 2, v[84:85]
	global_load_dword v147, v[180:181], off
	global_load_dword v146, v[180:181], off offset:256
	global_load_dword v149, v[180:181], off offset:512
	global_load_dword v148, v[180:181], off offset:768
	global_load_dword v151, v[180:181], off offset:1024
	global_load_dword v150, v[180:181], off offset:1280
	global_load_dword v153, v[180:181], off offset:1536
	global_load_dword v152, v[180:181], off offset:1792
	global_load_dword v155, v[180:181], off offset:2048
	global_load_dword v154, v[180:181], off offset:2304
	global_load_dword v157, v[180:181], off offset:2560
	global_load_dword v156, v[180:181], off offset:2816
	global_load_dword v159, v[180:181], off offset:3072
	global_load_dword v158, v[180:181], off offset:3328
	global_load_dword v161, v[180:181], off offset:3584
	global_load_dword v160, v[180:181], off offset:3840
	v_add_u32_e32 v144, 0x400, v144
	v_pk_mul_f32 v[102:103], v[88:89], v[78:79] op_sel:[0,1] op_sel_hi:[1,0]
	v_pk_fma_f32 v[106:107], v[86:87], v[78:79], v[102:103] neg_lo:[0,0,1] neg_hi:[0,0,1]
	v_pk_fma_f32 v[78:79], v[86:87], v[78:79], v[102:103]
	v_mov_b32_e32 v79, v107
	s_waitcnt vmcnt(14)
	v_pk_add_f32 v[78:79], v[78:79], v[146:147]
	v_pk_mul_f32 v[102:103], v[88:89], v[78:79] op_sel:[0,1] op_sel_hi:[1,0]
	v_pk_fma_f32 v[106:107], v[86:87], v[78:79], v[102:103] neg_lo:[0,0,1] neg_hi:[0,0,1]
	v_pk_fma_f32 v[78:79], v[86:87], v[78:79], v[102:103]
	v_mov_b32_e32 v79, v107
	s_waitcnt vmcnt(12)
	v_pk_add_f32 v[78:79], v[78:79], v[148:149]
	v_pk_mul_f32 v[102:103], v[88:89], v[78:79] op_sel:[0,1] op_sel_hi:[1,0]
	v_pk_fma_f32 v[106:107], v[86:87], v[78:79], v[102:103] neg_lo:[0,0,1] neg_hi:[0,0,1]
	v_pk_fma_f32 v[78:79], v[86:87], v[78:79], v[102:103]
	v_mov_b32_e32 v79, v107
	s_waitcnt vmcnt(10)
	v_pk_add_f32 v[78:79], v[78:79], v[150:151]
	v_pk_mul_f32 v[102:103], v[88:89], v[78:79] op_sel:[0,1] op_sel_hi:[1,0]
	v_pk_fma_f32 v[106:107], v[86:87], v[78:79], v[102:103] neg_lo:[0,0,1] neg_hi:[0,0,1]
	v_pk_fma_f32 v[78:79], v[86:87], v[78:79], v[102:103]
	v_mov_b32_e32 v79, v107
	s_waitcnt vmcnt(8)
	v_pk_add_f32 v[78:79], v[78:79], v[152:153]
	v_pk_mul_f32 v[102:103], v[88:89], v[78:79] op_sel:[0,1] op_sel_hi:[1,0]
	v_pk_fma_f32 v[106:107], v[86:87], v[78:79], v[102:103] neg_lo:[0,0,1] neg_hi:[0,0,1]
	v_pk_fma_f32 v[78:79], v[86:87], v[78:79], v[102:103]
	v_mov_b32_e32 v79, v107
	s_waitcnt vmcnt(6)
	v_pk_add_f32 v[78:79], v[78:79], v[154:155]
	v_pk_mul_f32 v[102:103], v[88:89], v[78:79] op_sel:[0,1] op_sel_hi:[1,0]
	v_pk_fma_f32 v[106:107], v[86:87], v[78:79], v[102:103] neg_lo:[0,0,1] neg_hi:[0,0,1]
	v_pk_fma_f32 v[78:79], v[86:87], v[78:79], v[102:103]
	v_mov_b32_e32 v79, v107
	s_waitcnt vmcnt(4)
	v_pk_add_f32 v[78:79], v[78:79], v[156:157]
	v_pk_mul_f32 v[102:103], v[88:89], v[78:79] op_sel:[0,1] op_sel_hi:[1,0]
	v_pk_fma_f32 v[106:107], v[86:87], v[78:79], v[102:103] neg_lo:[0,0,1] neg_hi:[0,0,1]
	v_pk_fma_f32 v[78:79], v[86:87], v[78:79], v[102:103]
	v_mov_b32_e32 v79, v107
	s_waitcnt vmcnt(2)
	v_pk_add_f32 v[78:79], v[78:79], v[158:159]
	v_pk_mul_f32 v[102:103], v[88:89], v[78:79] op_sel:[0,1] op_sel_hi:[1,0]
	v_pk_fma_f32 v[106:107], v[86:87], v[78:79], v[102:103] neg_lo:[0,0,1] neg_hi:[0,0,1]
	v_pk_fma_f32 v[78:79], v[86:87], v[78:79], v[102:103]
	v_mov_b32_e32 v79, v107
	s_waitcnt vmcnt(0)
	v_pk_add_f32 v[78:79], v[78:79], v[160:161]
.Lhorner_4:
	s_bitcmp1_b32 s6, 2
	s_cbranch_scc0 .Lhorner_2
	v_lshl_add_u64 v[180:181], v[144:145], 2, v[84:85]
	global_load_dword v147, v[180:181], off
	global_load_dword v146, v[180:181], off offset:256
	global_load_dword v149, v[180:181], off offset:512
	global_load_dword v148, v[180:181], off offset:768
	global_load_dword v151, v[180:181], off offset:1024
	global_load_dword v150, v[180:181], off offset:1280
	global_load_dword v153, v[180:181], off offset:1536
	global_load_dword v152, v[180:181], off offset:1792
	v_add_u32_e32 v144, 0x200, v144
	v_pk_mul_f32 v[102:103], v[88:89], v[78:79] op_sel:[0,1] op_sel_hi:[1,0]
	v_pk_fma_f32 v[106:107], v[86:87], v[78:79], v[102:103] neg_lo:[0,0,1] neg_hi:[0,0,1]
	v_pk_fma_f32 v[78:79], v[86:87], v[78:79], v[102:103]
	v_mov_b32_e32 v79, v107
	s_waitcnt vmcnt(6)
	v_pk_add_f32 v[78:79], v[78:79], v[146:147]
	v_pk_mul_f32 v[102:103], v[88:89], v[78:79] op_sel:[0,1] op_sel_hi:[1,0]
	v_pk_fma_f32 v[106:107], v[86:87], v[78:79], v[102:103] neg_lo:[0,0,1] neg_hi:[0,0,1]
	v_pk_fma_f32 v[78:79], v[86:87], v[78:79], v[102:103]
	v_mov_b32_e32 v79, v107
	s_waitcnt vmcnt(4)
	v_pk_add_f32 v[78:79], v[78:79], v[148:149]
	v_pk_mul_f32 v[102:103], v[88:89], v[78:79] op_sel:[0,1] op_sel_hi:[1,0]
	v_pk_fma_f32 v[106:107], v[86:87], v[78:79], v[102:103] neg_lo:[0,0,1] neg_hi:[0,0,1]
	v_pk_fma_f32 v[78:79], v[86:87], v[78:79], v[102:103]
	v_mov_b32_e32 v79, v107
	s_waitcnt vmcnt(2)
	v_pk_add_f32 v[78:79], v[78:79], v[150:151]
	v_pk_mul_f32 v[102:103], v[88:89], v[78:79] op_sel:[0,1] op_sel_hi:[1,0]
	v_pk_fma_f32 v[106:107], v[86:87], v[78:79], v[102:103] neg_lo:[0,0,1] neg_hi:[0,0,1]
	v_pk_fma_f32 v[78:79], v[86:87], v[78:79], v[102:103]
	v_mov_b32_e32 v79, v107
	s_waitcnt vmcnt(0)
	v_pk_add_f32 v[78:79], v[78:79], v[152:153]
.Lhorner_2:
	s_bitcmp1_b32 s6, 1
	s_cbranch_scc0 .Lhorner_1
	v_lshl_add_u64 v[180:181], v[144:145], 2, v[84:85]
	global_load_dword v147, v[180:181], off
	global_load_dword v146, v[180:181], off offset:256
	global_load_dword v149, v[180:181], off offset:512
	global_load_dword v148, v[180:181], off offset:768
	v_add_u32_e32 v144, 0x100, v144
	v_pk_mul_f32 v[102:103], v[88:89], v[78:79] op_sel:[0,1] op_sel_hi:[1,0]
	v_pk_fma_f32 v[106:107], v[86:87], v[78:79], v[102:103] neg_lo:[0,0,1] neg_hi:[0,0,1]
	v_pk_fma_f32 v[78:79], v[86:87], v[78:79], v[102:103]
	v_mov_b32_e32 v79, v107
	s_waitcnt vmcnt(2)
	v_pk_add_f32 v[78:79], v[78:79], v[146:147]
	v_pk_mul_f32 v[102:103], v[88:89], v[78:79] op_sel:[0,1] op_sel_hi:[1,0]
	v_pk_fma_f32 v[106:107], v[86:87], v[78:79], v[102:103] neg_lo:[0,0,1] neg_hi:[0,0,1]
	v_pk_fma_f32 v[78:79], v[86:87], v[78:79], v[102:103]
	v_mov_b32_e32 v79, v107
	s_waitcnt vmcnt(0)
	v_pk_add_f32 v[78:79], v[78:79], v[148:149]
.Lhorner_1:
	s_bitcmp1_b32 s6, 0
	s_cbranch_scc0 .LBB0_531
	v_lshl_add_u64 v[180:181], v[144:145], 2, v[84:85]
	global_load_dword v147, v[180:181], off
	global_load_dword v146, v[180:181], off offset:256
	v_add_u32_e32 v144, 0x80, v144
	v_pk_mul_f32 v[102:103], v[88:89], v[78:79] op_sel:[0,1] op_sel_hi:[1,0]
	v_pk_fma_f32 v[106:107], v[86:87], v[78:79], v[102:103] neg_lo:[0,0,1] neg_hi:[0,0,1]
	v_pk_fma_f32 v[78:79], v[86:87], v[78:79], v[102:103]
	v_mov_b32_e32 v79, v107
	s_waitcnt vmcnt(0)
	v_pk_add_f32 v[78:79], v[78:79], v[146:147]
